# strategy 2 / 7.3: P3 prep C_loc stores widened - MFMA operands swapped so each lane stores 16 contiguous bytes (8 dwordx4 instead of 32 dword stores per lane per item)
# speedup vs baseline: 1.0070x; 1.0020x over previous
.LBB0_365:
	s_waitcnt vmcnt(0)
	ds_read2st64_b32 v[2:3], v194 offset1:2
	v_cvt_pk_bf16_f32 v4, v89, v147
	s_mul_i32 s4, s52, 0x82
	v_lshlrev_b32_e32 v4, 16, v4
	s_add_i32 s4, s4, s51
	s_waitcnt lgkmcnt(0)
	v_mul_f32_e32 v5, v2, v4
	v_mul_f32_e32 v4, v3, v4
	v_cvt_pk_bf16_f32 v5, v5, v147
	ds_write_b16 v195, v5 offset:34816
	v_cvt_pk_bf16_f32 v4, v4, v147
	ds_write_b16 v195, v4 offset:52224
	v_cvt_pk_bf16_f32 v4, v86, v147
	s_ashr_i32 s5, s4, 31
	v_lshlrev_b32_e32 v4, 16, v4
	v_mul_f32_e32 v5, v2, v4
	v_mul_f32_e32 v4, v3, v4
	v_cvt_pk_bf16_f32 v5, v5, v147
	ds_write_b16 v195, v5 offset:35088
	v_cvt_pk_bf16_f32 v4, v4, v147
	ds_write_b16 v195, v4 offset:52496
	v_cvt_pk_bf16_f32 v4, v63, v147
	s_lshl_b64 s[16:17], s[4:5], 15
	v_lshlrev_b32_e32 v4, 16, v4
	v_mul_f32_e32 v5, v2, v4
	v_mul_f32_e32 v4, v3, v4
	v_cvt_pk_bf16_f32 v5, v5, v147
	ds_write_b16 v195, v5 offset:35360
	v_cvt_pk_bf16_f32 v4, v4, v147
	ds_write_b16 v195, v4 offset:52768
	v_cvt_pk_bf16_f32 v4, v88, v147
	s_add_u32 s16, s41, s16
	v_lshlrev_b32_e32 v4, 16, v4
	v_mul_f32_e32 v5, v2, v4
	v_mul_f32_e32 v4, v3, v4
	v_cvt_pk_bf16_f32 v5, v5, v147
	ds_write_b16 v195, v5 offset:35632
	v_cvt_pk_bf16_f32 v4, v4, v147
	ds_write_b16 v195, v4 offset:53040
	v_cvt_pk_bf16_f32 v4, v65, v147
	s_addc_u32 s17, s42, s17
	v_lshlrev_b32_e32 v4, 16, v4
	v_mul_f32_e32 v5, v2, v4
	v_mul_f32_e32 v4, v3, v4
	v_cvt_pk_bf16_f32 v5, v5, v147
	ds_write_b16 v195, v5 offset:35904
	v_cvt_pk_bf16_f32 v4, v4, v147
	ds_write_b16 v195, v4 offset:53312
	v_cvt_pk_bf16_f32 v4, v62, v147
	v_lshl_add_u64 v[42:43], s[16:17], 0, v[164:165]
	v_lshlrev_b32_e32 v4, 16, v4
	v_mul_f32_e32 v5, v2, v4
	v_mul_f32_e32 v4, v3, v4
	v_cvt_pk_bf16_f32 v5, v5, v147
	ds_write_b16 v195, v5 offset:36176
	v_cvt_pk_bf16_f32 v4, v4, v147
	ds_write_b16 v195, v4 offset:53584
	v_cvt_pk_bf16_f32 v4, v66, v147
	s_addk_i32 s4, 0x410
	v_lshlrev_b32_e32 v4, 16, v4
	v_mul_f32_e32 v5, v2, v4
	v_mul_f32_e32 v4, v3, v4
	v_cvt_pk_bf16_f32 v5, v5, v147
	ds_write_b16 v195, v5 offset:36448
	v_cvt_pk_bf16_f32 v4, v4, v147
	ds_write_b16 v195, v4 offset:53856
	v_cvt_pk_bf16_f32 v4, v64, v147
	s_ashr_i32 s5, s4, 31
	v_lshlrev_b32_e32 v4, 16, v4
	v_mul_f32_e32 v5, v2, v4
	v_mul_f32_e32 v4, v3, v4
	v_cvt_pk_bf16_f32 v5, v5, v147
	ds_write_b16 v195, v5 offset:36720
	v_cvt_pk_bf16_f32 v4, v4, v147
	ds_write_b16 v195, v4 offset:54128
	v_cvt_pk_bf16_f32 v4, v106, v147
	s_lshl_b64 s[4:5], s[4:5], 15
	v_lshlrev_b32_e32 v4, 16, v4
	v_mul_f32_e32 v5, v2, v4
	v_mul_f32_e32 v4, v3, v4
	v_cvt_pk_bf16_f32 v5, v5, v147
	ds_write_b16 v195, v5 offset:36992
	v_cvt_pk_bf16_f32 v4, v4, v147
	ds_write_b16 v195, v4 offset:54400
	v_cvt_pk_bf16_f32 v4, v102, v147
	s_add_u32 s4, s41, s4
	v_lshlrev_b32_e32 v4, 16, v4
	v_mul_f32_e32 v5, v2, v4
	v_mul_f32_e32 v4, v3, v4
	v_cvt_pk_bf16_f32 v5, v5, v147
	ds_write_b16 v195, v5 offset:37264
	v_cvt_pk_bf16_f32 v4, v4, v147
	ds_write_b16 v195, v4 offset:54672
	v_cvt_pk_bf16_f32 v4, v107, v147
	s_addc_u32 s5, s42, s5
	v_lshlrev_b32_e32 v4, 16, v4
	v_mul_f32_e32 v5, v2, v4
	v_mul_f32_e32 v4, v3, v4
	v_cvt_pk_bf16_f32 v5, v5, v147
	ds_write_b16 v195, v5 offset:37536
	v_cvt_pk_bf16_f32 v4, v4, v147
	ds_write_b16 v195, v4 offset:54944
	v_cvt_pk_bf16_f32 v4, v103, v147
	s_nop 0
	v_lshlrev_b32_e32 v4, 16, v4
	v_mul_f32_e32 v5, v2, v4
	v_mul_f32_e32 v4, v3, v4
	v_cvt_pk_bf16_f32 v5, v5, v147
	ds_write_b16 v195, v5 offset:37808
	v_cvt_pk_bf16_f32 v4, v4, v147
	ds_write_b16 v195, v4 offset:55216
	v_cvt_pk_bf16_f32 v4, v108, v147
	s_nop 0
	v_lshlrev_b32_e32 v4, 16, v4
	v_mul_f32_e32 v5, v2, v4
	v_mul_f32_e32 v4, v3, v4
	v_cvt_pk_bf16_f32 v5, v5, v147
	ds_write_b16 v195, v5 offset:38080
	v_cvt_pk_bf16_f32 v4, v4, v147
	ds_write_b16 v195, v4 offset:55488
	v_cvt_pk_bf16_f32 v4, v104, v147
	s_nop 0
	v_lshlrev_b32_e32 v4, 16, v4
	v_mul_f32_e32 v5, v2, v4
	v_mul_f32_e32 v4, v3, v4
	v_cvt_pk_bf16_f32 v5, v5, v147
	ds_write_b16 v195, v5 offset:38352
	v_cvt_pk_bf16_f32 v4, v4, v147
	ds_write_b16 v195, v4 offset:55760
	v_cvt_pk_bf16_f32 v4, v87, v147
	s_nop 0
	v_lshlrev_b32_e32 v4, 16, v4
	v_mul_f32_e32 v5, v2, v4
	v_mul_f32_e32 v4, v3, v4
	v_cvt_pk_bf16_f32 v5, v5, v147
	ds_write_b16 v195, v5 offset:38624
	v_cvt_pk_bf16_f32 v4, v4, v147
	ds_write_b16 v195, v4 offset:56032
	v_cvt_pk_bf16_f32 v4, v105, v147
	s_nop 0
	v_lshlrev_b32_e32 v4, 16, v4
	v_mul_f32_e32 v2, v2, v4
	v_cvt_pk_bf16_f32 v2, v2, v147
	ds_write_b16 v195, v2 offset:38896
	v_mul_f32_e32 v2, v3, v4
	v_cvt_pk_bf16_f32 v2, v2, v147
	ds_write_b16 v195, v2 offset:56304
	s_waitcnt lgkmcnt(0)
	s_barrier
	ds_read_b128 v[2:5], v199
	ds_read_b128 v[6:9], v199 offset:64
	ds_read_b128 v[18:21], v199 offset:128
	ds_read_b128 v[22:25], v199 offset:192
	ds_read_b128 v[10:13], v200 offset:34816
	ds_read_b128 v[14:17], v200 offset:34880
	ds_read_b128 v[26:29], v200 offset:34944
	ds_read_b128 v[30:33], v200 offset:35008
	v_and_b32_e32 v42, 15, v206
	v_lshrrev_b32_e32 v43, 6, v0
	v_lshl_add_u32 v42, v43, 4, v42
	v_lshrrev_b32_e32 v43, 4, v206
	v_lshlrev_b32_e32 v42, 8, v42
	v_lshl_add_u32 v42, v43, 4, v42
	s_waitcnt lgkmcnt(0)
	v_mfma_f32_16x16x32_bf16 v[34:37], v[10:13], v[2:5], 0
	v_mfma_f32_16x16x32_bf16 v[34:37], v[14:17], v[6:9], v[34:37]
	v_mfma_f32_16x16x32_bf16 v[34:37], v[26:29], v[18:21], v[34:37]
	v_mfma_f32_16x16x32_bf16 v[34:37], v[30:33], v[22:25], v[34:37]
	ds_read_b128 v[10:13], v200 offset:39168
	ds_read_b128 v[14:17], v200 offset:39232
	ds_read_b128 v[26:29], v200 offset:39296
	ds_read_b128 v[30:33], v200 offset:39360
	s_waitcnt lgkmcnt(0)
	v_mfma_f32_16x16x32_bf16 v[38:41], v[10:13], v[2:5], 0
	v_mfma_f32_16x16x32_bf16 v[38:41], v[14:17], v[6:9], v[38:41]
	v_mfma_f32_16x16x32_bf16 v[38:41], v[26:29], v[18:21], v[38:41]
	v_mfma_f32_16x16x32_bf16 v[38:41], v[30:33], v[22:25], v[38:41]
	ds_read_b128 v[10:13], v200 offset:43520
	ds_read_b128 v[14:17], v200 offset:43584
	ds_read_b128 v[26:29], v200 offset:43648
	ds_read_b128 v[30:33], v200 offset:43712
	global_store_dwordx4 v42, v[34:37], s[16:17]
	s_nop 1
	s_waitcnt lgkmcnt(0)
	v_mfma_f32_16x16x32_bf16 v[34:37], v[10:13], v[2:5], 0
	v_mfma_f32_16x16x32_bf16 v[34:37], v[14:17], v[6:9], v[34:37]
	v_mfma_f32_16x16x32_bf16 v[34:37], v[26:29], v[18:21], v[34:37]
	v_mfma_f32_16x16x32_bf16 v[34:37], v[30:33], v[22:25], v[34:37]
	ds_read_b128 v[10:13], v200 offset:47872
	ds_read_b128 v[14:17], v200 offset:47936
	ds_read_b128 v[26:29], v200 offset:48000
	ds_read_b128 v[30:33], v200 offset:48064
	global_store_dwordx4 v42, v[38:41], s[16:17] offset:64
	s_nop 1
	s_waitcnt lgkmcnt(0)
	v_mfma_f32_16x16x32_bf16 v[38:41], v[10:13], v[2:5], 0
	v_mfma_f32_16x16x32_bf16 v[38:41], v[14:17], v[6:9], v[38:41]
	v_mfma_f32_16x16x32_bf16 v[38:41], v[26:29], v[18:21], v[38:41]
	v_mfma_f32_16x16x32_bf16 v[38:41], v[30:33], v[22:25], v[38:41]
	ds_read_b128 v[10:13], v200 offset:52224
	ds_read_b128 v[14:17], v200 offset:52288
	ds_read_b128 v[26:29], v200 offset:52352
	ds_read_b128 v[30:33], v200 offset:52416
	global_store_dwordx4 v42, v[34:37], s[16:17] offset:128
	s_nop 1
	s_waitcnt lgkmcnt(0)
	v_mfma_f32_16x16x32_bf16 v[34:37], v[10:13], v[2:5], 0
	v_mfma_f32_16x16x32_bf16 v[34:37], v[14:17], v[6:9], v[34:37]
	v_mfma_f32_16x16x32_bf16 v[34:37], v[26:29], v[18:21], v[34:37]
	v_mfma_f32_16x16x32_bf16 v[34:37], v[30:33], v[22:25], v[34:37]
	ds_read_b128 v[10:13], v200 offset:56576
	ds_read_b128 v[14:17], v200 offset:56640
	ds_read_b128 v[26:29], v200 offset:56704
	ds_read_b128 v[30:33], v200 offset:56768
	global_store_dwordx4 v42, v[38:41], s[16:17] offset:192
	s_nop 1
	s_waitcnt lgkmcnt(0)
	v_mfma_f32_16x16x32_bf16 v[38:41], v[10:13], v[2:5], 0
	v_mfma_f32_16x16x32_bf16 v[38:41], v[14:17], v[6:9], v[38:41]
	v_mfma_f32_16x16x32_bf16 v[38:41], v[26:29], v[18:21], v[38:41]
	v_mfma_f32_16x16x32_bf16 v[38:41], v[30:33], v[22:25], v[38:41]
	ds_read_b128 v[10:13], v200 offset:60928
	ds_read_b128 v[14:17], v200 offset:60992
	ds_read_b128 v[26:29], v200 offset:61056
	ds_read_b128 v[30:33], v200 offset:61120
	global_store_dwordx4 v42, v[34:37], s[4:5]
	s_nop 1
	s_waitcnt lgkmcnt(0)
	v_mfma_f32_16x16x32_bf16 v[34:37], v[10:13], v[2:5], 0
	v_mfma_f32_16x16x32_bf16 v[34:37], v[14:17], v[6:9], v[34:37]
	v_mfma_f32_16x16x32_bf16 v[34:37], v[26:29], v[18:21], v[34:37]
	v_mfma_f32_16x16x32_bf16 v[34:37], v[30:33], v[22:25], v[34:37]
	ds_read_b128 v[10:13], v200 offset:65280
	ds_read_b128 v[14:17], v200 offset:65344
	ds_read_b128 v[26:29], v200 offset:65408
	ds_read_b128 v[30:33], v200 offset:65472
	global_store_dwordx4 v42, v[38:41], s[4:5] offset:64
	s_nop 1
	s_waitcnt lgkmcnt(0)
	v_mfma_f32_16x16x32_bf16 v[38:41], v[10:13], v[2:5], 0
	v_mfma_f32_16x16x32_bf16 v[38:41], v[14:17], v[6:9], v[38:41]
	v_mfma_f32_16x16x32_bf16 v[38:41], v[26:29], v[18:21], v[38:41]
	v_mfma_f32_16x16x32_bf16 v[38:41], v[30:33], v[22:25], v[38:41]
	s_nop 7
	global_store_dwordx4 v42, v[34:37], s[4:5] offset:128
	s_nop 1
	s_nop 7
	s_nop 1
	global_store_dwordx4 v42, v[38:41], s[4:5] offset:192
	s_nop 1
	s_and_saveexec_b64 s[4:5], s[14:15]
	s_cbranch_execz .LBB0_342
	v_mov_b32_e32 v2, 0
	s_mov_b32 s16, 0
